# mLSTM chain unit (chains + Q fragment loader) rewritten by hand: counted waits, four chunks of operands in flight, no per-iteration drain
# speedup vs baseline: 1.0139x; 1.0024x over previous
; #define LAS __attribute__((address_space(3)))
; #define M2_FETCH(dst, c_) do { _Pragma("unroll") for (int i = 0; i < 12; ++i) dst[i] = __builtin_nontemporal_load((const u32x4_t*)(pkg0 + (size_t)(c_) * MLP_BYTES + MLP_QF + i * 1024 + lane * 16)); } while (0)
; DI void mlstm_m2_unit(const Args& A, LAS unsigned char* lds, int u, int tid, int wave, int lane) {
;     bf16* num = (bf16*)(A.ws + WS_MLNUM); float* den = (float*)(A.ws + WS_MLDEN);
;     const int dir = u / 32, b = (u % 32) / 4, hh = u % 4; const int fr = lane & 15, qd = lane >> 4;
;     const unsigned char* pkg0 = A.ws + WS_MLPKG + (size_t)u * 32 * MLP_BYTES;
;     volatile LAS unsigned* ready = (volatile LAS unsigned*)(lds + M2_CTL); volatile LAS unsigned* consumed = ready + 8;
;     __syncthreads();
;     if (tid < 16) ready[tid] = 0u;
;     __syncthreads();
;     if (wave == 7) {
;         u32x4_t f0[12], f1[12], f2[12];
;     ...
;         M2_FETCH(f0, 0); M2_FETCH(f1, 1);
;         for (int c = 0; c < 30; c += 3) { M2_FETCH(f2, c + 2); M2_PUBLISH(f0, c); M2_FETCH(f0, c + 3); M2_PUBLISH(f1, c + 1); M2_FETCH(f1, c + 4); M2_PUBLISH(f2, c + 2); }
;         M2_PUBLISH(f0, 30); M2_PUBLISH(f1, 31);
;     ...
;     } else {
;         const int nt = wave; f32x4 C[6];
; #pragma unroll
;         for (int kt = 0; kt < 6; ++kt) C[kt] = (f32x4){0.f, 0.f, 0.f, 0.f};
;         M2Small s0, s1, s2, s3;
;         m2_load_small(s0, pkg0, nt, lane); m2_load_small(s1, pkg0 + MLP_BYTES, nt, lane); m2_load_small(s2, pkg0 + 2 * (size_t)MLP_BYTES, nt, lane); m2_load_small(s3, pkg0 + 3 * (size_t)MLP_BYTES, nt, lane);
; template <int l> DI void run_layer(const Args& A, LAS unsigned char* lds, const XcdBarrier& bar, int lo, int hi, int G, int bid, int tid, int lane, int wave, int gw, int ngw, int gtid, int nthr) {
;     ...
;           for (int rep = 0; rep < 1 + ((MK_DUP >> 15) & 1); ++rep) for (int u = bid; u < 96 + 64; u += G) { if (u >= 96) mlstm_m2_unit(A, lds, u - 96, tid, wave, lane); });
.LBB0_701:
	s_mov_b32 s6, s92
.Lm20_uloop:
	s_cmpk_gt_i32 s6, 0x9f
	s_cbranch_scc1 .LBB0_957
	s_cmpk_lt_i32 s6, 0x60
	s_cbranch_scc1 .Lm20_unext
	s_add_i32 s7, s6, 0xffffffa0
	s_lshr_b32 s8, s7, 5
	s_bfe_u32 s9, s7, 0x30002
	s_and_b32 s10, s7, 3
	v_readlane_b32 s11, v235, 52
	v_readlane_b32 s2, v235, 9
	v_readlane_b32 s3, v235, 10
	s_mul_i32 s12, s7, 0x17a000
	s_add_u32 s12, s12, 0x3fa00000
	s_add_u32 s14, s2, s12
	s_addc_u32 s15, s3, 0
	s_waitcnt vmcnt(0) lgkmcnt(0)
	s_barrier
	v_cmp_gt_u32_e32 vcc, 16, v0
	v_lshl_add_u32 v2, v0, 2, 0
	v_add_u32_e32 v2, 0x18000, v2
	v_mov_b32_e32 v3, 0
	s_and_saveexec_b64 s[16:17], vcc
	ds_write_b32 v2, v3
	s_mov_b64 exec, s[16:17]
	s_waitcnt lgkmcnt(0)
	s_barrier
	v_cmp_eq_u32_e64 s[72:73], 0, v146
	s_cmp_eq_u32 s11, 7
	s_cbranch_scc1 .Lm20_loader
	v_and_b32_e32 v12, 15, v146
	v_lshrrev_b32_e32 v13, 4, v146
	v_lshlrev_b32_e32 v14, 3, v146
	s_lshl_b32 s16, s11, 11
	s_mul_i32 s17, s11, 0xc00
	s_add_i32 s16, s16, 0x3000
	s_add_i32 s17, s17, 0x6800
	v_add_u32_e32 v4, s16, v14
	v_add_u32_e32 v5, s17, v14
	v_lshlrev_b32_e32 v6, 2, v146
	v_add_u32_e32 v6, 0xbc00, v6
	v_lshlrev_b32_e32 v9, 4, v146
	s_cmp_eq_u32 s8, 0
	s_cselect_b32 s18, 1, -1
	v_mul_lo_u32 v15, v12, s18
	s_movk_i32 s19, 0x300
	v_mul_lo_u32 v7, v15, s19
	s_mul_i32 s16, s10, 0xc0
	s_lshl_b32 s17, s11, 5
	s_add_i32 s16, s16, s17
	v_lshl_add_u32 v16, v13, 3, s16
	v_add_u32_e32 v7, v7, v16
	v_lshlrev_b32_e32 v8, 4, v15
	s_lshl_b32 s16, s10, 2
	v_add_u32_e32 v8, s16, v8
	s_lshl_b32 s76, s8, 14
	s_lshl_b32 s16, s9, 11
	s_add_i32 s76, s76, s16
	s_cmp_eq_u32 s8, 0
	s_cselect_b32 s16, 0, 0x7ff
	s_add_i32 s76, s76, s16
	s_lshl_b32 s77, s18, 4
	s_add_u32 s78, s2, 0x51400000
	s_addc_u32 s79, s3, 0
	s_add_u32 s80, s2, 0x54400000
	s_addc_u32 s81, s3, 0
	v_cmp_gt_u32_e64 s[74:75], 16, v146
	s_lshl_b32 s82, s11, 2
	s_add_i32 s82, s82, 0x18020
	v_mov_b32_e32 v20, 0
	v_mov_b32_e32 v21, 0
	v_mov_b32_e32 v22, 0
	v_mov_b32_e32 v23, 0
	v_mov_b32_e32 v24, 0
	v_mov_b32_e32 v25, 0
	v_mov_b32_e32 v26, 0
	v_mov_b32_e32 v27, 0
	v_mov_b32_e32 v28, 0
	v_mov_b32_e32 v29, 0
	v_mov_b32_e32 v30, 0
	v_mov_b32_e32 v31, 0
	v_mov_b32_e32 v32, 0
	v_mov_b32_e32 v33, 0
	v_mov_b32_e32 v34, 0
	v_mov_b32_e32 v35, 0
	v_mov_b32_e32 v36, 0
	v_mov_b32_e32 v37, 0
	v_mov_b32_e32 v38, 0
	v_mov_b32_e32 v39, 0
	v_mov_b32_e32 v40, 0
	v_mov_b32_e32 v41, 0
	v_mov_b32_e32 v42, 0
	v_mov_b32_e32 v43, 0
	s_mov_b32 s30, 0
	s_mul_i32 s27, s30, 0xbd00
	s_add_u32 s28, s14, s27
	s_addc_u32 s29, s15, 0
	global_load_dwordx2 v[120:121], v4, s[28:29] nt
	global_load_dwordx2 v[122:123], v4, s[28:29] offset:512 nt
	global_load_dwordx2 v[124:125], v4, s[28:29] offset:1024 nt
	global_load_dwordx2 v[126:127], v4, s[28:29] offset:1536 nt
	global_load_dwordx2 v[128:129], v5, s[28:29] nt
	global_load_dwordx2 v[130:131], v5, s[28:29] offset:512 nt
	global_load_dwordx2 v[132:133], v5, s[28:29] offset:1024 nt
	global_load_dwordx2 v[134:135], v5, s[28:29] offset:1536 nt
	global_load_dwordx2 v[136:137], v5, s[28:29] offset:2048 nt
	global_load_dwordx2 v[138:139], v5, s[28:29] offset:2560 nt
	global_load_dword v140, v6, s[28:29]
	s_mov_b32 s30, 1
	s_mul_i32 s27, s30, 0xbd00
	s_add_u32 s28, s14, s27
	s_addc_u32 s29, s15, 0
	global_load_dwordx2 v[148:149], v4, s[28:29] nt
	global_load_dwordx2 v[150:151], v4, s[28:29] offset:512 nt
	global_load_dwordx2 v[152:153], v4, s[28:29] offset:1024 nt
	global_load_dwordx2 v[154:155], v4, s[28:29] offset:1536 nt
	global_load_dwordx2 v[156:157], v5, s[28:29] nt
	global_load_dwordx2 v[158:159], v5, s[28:29] offset:512 nt
	global_load_dwordx2 v[160:161], v5, s[28:29] offset:1024 nt
	global_load_dwordx2 v[162:163], v5, s[28:29] offset:1536 nt
	global_load_dwordx2 v[164:165], v5, s[28:29] offset:2048 nt
	global_load_dwordx2 v[166:167], v5, s[28:29] offset:2560 nt
	global_load_dword v168, v6, s[28:29]
	s_mov_b32 s30, 2
	s_mul_i32 s27, s30, 0xbd00
	s_add_u32 s28, s14, s27
	s_addc_u32 s29, s15, 0
	global_load_dwordx2 v[172:173], v4, s[28:29] nt
	global_load_dwordx2 v[174:175], v4, s[28:29] offset:512 nt
	global_load_dwordx2 v[176:177], v4, s[28:29] offset:1024 nt
	global_load_dwordx2 v[178:179], v4, s[28:29] offset:1536 nt
	global_load_dwordx2 v[180:181], v5, s[28:29] nt
	global_load_dwordx2 v[182:183], v5, s[28:29] offset:512 nt
	global_load_dwordx2 v[184:185], v5, s[28:29] offset:1024 nt
	global_load_dwordx2 v[186:187], v5, s[28:29] offset:1536 nt
	global_load_dwordx2 v[188:189], v5, s[28:29] offset:2048 nt
	global_load_dwordx2 v[190:191], v5, s[28:29] offset:2560 nt
	global_load_dword v192, v6, s[28:29]
	s_mov_b32 s30, 3
	s_mul_i32 s27, s30, 0xbd00
	s_add_u32 s28, s14, s27
	s_addc_u32 s29, s15, 0
	global_load_dwordx2 v[194:195], v4, s[28:29] nt
	global_load_dwordx2 v[196:197], v4, s[28:29] offset:512 nt
	global_load_dwordx2 v[198:199], v4, s[28:29] offset:1024 nt
	global_load_dwordx2 v[200:201], v4, s[28:29] offset:1536 nt
	global_load_dwordx2 v[202:203], v5, s[28:29] nt
	global_load_dwordx2 v[204:205], v5, s[28:29] offset:512 nt
	global_load_dwordx2 v[206:207], v5, s[28:29] offset:1024 nt
	global_load_dwordx2 v[208:209], v5, s[28:29] offset:1536 nt
	global_load_dwordx2 v[210:211], v5, s[28:29] offset:2048 nt
	global_load_dwordx2 v[212:213], v5, s[28:29] offset:2560 nt
	global_load_dword v214, v6, s[28:29]
	s_mov_b32 s31, 0
	v_mov_b32_e32 v10, 0x18000
	ds_read_b32 v11, v10
.Lm20_cloop:
	s_add_i32 s32, s31, 0
	s_add_i32 s33, s32, 1
	s_and_b32 s34, s32, 7
	s_mul_i32 s35, s34, 0x3000
	v_cvt_pk_bf16_f32 v44, v20, v21
	v_cvt_pk_bf16_f32 v45, v22, v23
	v_cvt_pk_bf16_f32 v46, v24, v25
	v_cvt_pk_bf16_f32 v47, v26, v27
	v_cvt_pk_bf16_f32 v48, v28, v29
	v_cvt_pk_bf16_f32 v49, v30, v31
	v_cvt_pk_bf16_f32 v50, v32, v33
	v_cvt_pk_bf16_f32 v51, v34, v35
	v_cvt_pk_bf16_f32 v52, v36, v37
	v_cvt_pk_bf16_f32 v53, v38, v39
	v_cvt_pk_bf16_f32 v54, v40, v41
	v_cvt_pk_bf16_f32 v55, v42, v43
	s_waitcnt lgkmcnt(0)
	v_cmp_eq_u32_e32 vcc, s33, v11
	s_cbranch_vccnz .Lm20_s0_rdy
	s_mov_b32 s36, 0x400000
; #define LAS __attribute__((address_space(3)))
; DI unsigned cvtpk(float lo, float hi) { const f2_t v = {lo, hi}; return __builtin_bit_cast(unsigned, __builtin_convertvector(v, bf2_t)); }
; #define MFMA16(a, b, c) __builtin_amdgcn_mfma_f32_16x16x32_bf16((a), (b), (c), 0, 0, 0)
; DI f32x4 unpk4(const u32x2_t w) { return (f32x4){__uint_as_float(w.x << 16), __uint_as_float(w.x & 0xffff0000u), __uint_as_float(w.y << 16), __uint_as_float(w.y & 0xffff0000u)}; }
; DI void m2_step(const M2Small& o, const LAS unsigned char* slot, f32x4 (&C)[6], bf16* num, float* den, int dir, int b, int hh, int nt, int c, int lane, int fr, int qd) {
;     union { unsigned u[4]; bf16x8_t v; } sB[3];
; #pragma unroll
;     for (int i = 0; i < 3; ++i) { sB[i].u[0] = cvtpk(C[2 * i][0], C[2 * i][1]); sB[i].u[1] = cvtpk(C[2 * i][2], C[2 * i][3]); sB[i].u[2] = cvtpk(C[2 * i + 1][0], C[2 * i + 1][1]); sB[i].u[3] = cvtpk(C[2 * i + 1][2], C[2 * i + 1][3]); }
; #pragma unroll
;     for (int jt = 0; jt < 4; ++jt) { f32x4 acc = unpk4(o.ni[jt]);
; #pragma unroll
;         for (int i = 0; i < 3; ++i) { const bf16x8_t qf = *(const LAS bf16x8_t*)(slot + (3 * jt + i) * 1024 + lane * 16); acc = MFMA16(sB[i].v, qf, acc); }
;         { const int jj = 16 * jt + fr; const int tt = dir ? SEQ - 1 - (c * 64 + jj) : c * 64 + jj; const size_t tok = (size_t)b * SEQ + tt;
;           if (nt < 6) { u32x2_t w; w.x = cvtpk(acc[0], acc[1]); w.y = cvtpk(acc[2], acc[3]); *(u32x2_t*)(num + ((size_t)dir * NT + tok) * MW + hh * 96 + 16 * nt + 4 * qd) = w; }
;           else if (qd == 0) den[((size_t)dir * NT + tok) * 4 + hh] = acc[0]; } }
; #pragma unroll
;     for (int kt = 0; kt < 6; ++kt) C[kt] = C[kt] * o.dec + unpk4(o.uu[kt]);
.Lm20_s0_spin:
	s_sleep 1
	ds_read_b32 v11, v10
	s_add_i32 s36, s36, -1
	s_cmp_eq_u32 s36, 0
	s_cbranch_scc1 .Lm20_s0_rdy
	s_waitcnt lgkmcnt(0)
	v_cmp_eq_u32_e32 vcc, s33, v11
	s_cbranch_vccz .Lm20_s0_spin
.Lm20_s0_rdy:
	v_add_u32_e32 v12, s35, v9
	ds_read_b128 v[72:75], v12 offset:0
	ds_read_b128 v[76:79], v12 offset:3072
	ds_read_b128 v[80:83], v12 offset:6144
	ds_read_b128 v[84:87], v12 offset:9216
	ds_read_b128 v[88:91], v12 offset:1024
	ds_read_b128 v[92:95], v12 offset:4096
	ds_read_b128 v[96:99], v12 offset:7168
	ds_read_b128 v[100:103], v12 offset:10240
	ds_read_b128 v[104:107], v12 offset:2048
	ds_read_b128 v[108:111], v12 offset:5120
	ds_read_b128 v[112:115], v12 offset:8192
	ds_read_b128 v[116:119], v12 offset:11264
	s_cmp_eq_u32 s31, 0
	s_cbranch_scc1 .Lm20_w0_first
	s_cmp_eq_u32 s31, 28
	s_cbranch_scc1 .Lm20_w0_last
	s_waitcnt vmcnt(45)
	s_branch .Lm20_w0_done
.Lm20_w0_first:
	s_waitcnt vmcnt(33)
	s_branch .Lm20_w0_done
.Lm20_w0_last:
	s_waitcnt vmcnt(45)
.Lm20_w0_done:
	v_lshlrev_b32_e32 v56, 16, v120
	v_and_b32_e32 v57, 0xffff0000, v120
	v_lshlrev_b32_e32 v58, 16, v121
	v_and_b32_e32 v59, 0xffff0000, v121
	v_lshlrev_b32_e32 v60, 16, v122
	v_and_b32_e32 v61, 0xffff0000, v122
	v_lshlrev_b32_e32 v62, 16, v123
	v_and_b32_e32 v63, 0xffff0000, v123
	v_lshlrev_b32_e32 v64, 16, v124
	v_and_b32_e32 v65, 0xffff0000, v124
	v_lshlrev_b32_e32 v66, 16, v125
	v_and_b32_e32 v67, 0xffff0000, v125
	v_lshlrev_b32_e32 v68, 16, v126
	v_and_b32_e32 v69, 0xffff0000, v126
	v_lshlrev_b32_e32 v70, 16, v127
	v_and_b32_e32 v71, 0xffff0000, v127
	s_waitcnt lgkmcnt(11)
	v_mfma_f32_16x16x32_bf16 v[56:59], v[44:47], v[72:75], v[56:59]
	s_waitcnt lgkmcnt(10)
	v_mfma_f32_16x16x32_bf16 v[60:63], v[44:47], v[76:79], v[60:63]
	s_waitcnt lgkmcnt(9)
	v_mfma_f32_16x16x32_bf16 v[64:67], v[44:47], v[80:83], v[64:67]
	s_waitcnt lgkmcnt(8)
	v_mfma_f32_16x16x32_bf16 v[68:71], v[44:47], v[84:87], v[68:71]
	s_add_i32 s37, s32, 1
	s_and_b32 s37, s37, 7
	s_lshl_b32 s37, s37, 2
	s_add_i32 s37, s37, 0x18000
	v_mov_b32_e32 v10, s37
	s_waitcnt lgkmcnt(7)
	v_mfma_f32_16x16x32_bf16 v[56:59], v[48:51], v[88:91], v[56:59]
	s_waitcnt lgkmcnt(6)
	v_mfma_f32_16x16x32_bf16 v[60:63], v[48:51], v[92:95], v[60:63]
	s_waitcnt lgkmcnt(5)
	v_mfma_f32_16x16x32_bf16 v[64:67], v[48:51], v[96:99], v[64:67]
	s_waitcnt lgkmcnt(4)
	v_mfma_f32_16x16x32_bf16 v[68:71], v[48:51], v[100:103], v[68:71]
	s_waitcnt lgkmcnt(3)
	v_mfma_f32_16x16x32_bf16 v[56:59], v[52:55], v[104:107], v[56:59]
	s_waitcnt lgkmcnt(2)
	v_mfma_f32_16x16x32_bf16 v[60:63], v[52:55], v[108:111], v[60:63]
	s_waitcnt lgkmcnt(1)
	v_mfma_f32_16x16x32_bf16 v[64:67], v[52:55], v[112:115], v[64:67]
	s_waitcnt lgkmcnt(0)
	v_mfma_f32_16x16x32_bf16 v[68:71], v[52:55], v[116:119], v[68:71]
	s_mov_b64 exec, s[72:73]
	v_mov_b32_e32 v13, s82
	v_mov_b32_e32 v14, s33
	ds_write_b32 v13, v14
	s_mov_b64 exec, -1
	ds_read_b32 v11, v10
	v_mov_b32_e32 v141, v140
	v_lshlrev_b32_e32 v16, 16, v128
	v_and_b32_e32 v17, 0xffff0000, v128
	v_lshlrev_b32_e32 v18, 16, v129
	v_and_b32_e32 v19, 0xffff0000, v129
	v_pk_fma_f32 v[20:21], v[140:141], v[20:21], v[16:17]
	v_pk_fma_f32 v[22:23], v[140:141], v[22:23], v[18:19]
	v_lshlrev_b32_e32 v16, 16, v130
	v_and_b32_e32 v17, 0xffff0000, v130
	v_lshlrev_b32_e32 v18, 16, v131
	v_and_b32_e32 v19, 0xffff0000, v131
	v_pk_fma_f32 v[24:25], v[140:141], v[24:25], v[16:17]
	v_pk_fma_f32 v[26:27], v[140:141], v[26:27], v[18:19]
	v_lshlrev_b32_e32 v16, 16, v132
	v_and_b32_e32 v17, 0xffff0000, v132
	v_lshlrev_b32_e32 v18, 16, v133
	v_and_b32_e32 v19, 0xffff0000, v133
	v_pk_fma_f32 v[28:29], v[140:141], v[28:29], v[16:17]
	v_pk_fma_f32 v[30:31], v[140:141], v[30:31], v[18:19]
	v_lshlrev_b32_e32 v16, 16, v134
	v_and_b32_e32 v17, 0xffff0000, v134
	v_lshlrev_b32_e32 v18, 16, v135
	v_and_b32_e32 v19, 0xffff0000, v135
	v_pk_fma_f32 v[32:33], v[140:141], v[32:33], v[16:17]
	v_pk_fma_f32 v[34:35], v[140:141], v[34:35], v[18:19]
	v_lshlrev_b32_e32 v16, 16, v136
	v_and_b32_e32 v17, 0xffff0000, v136
	v_lshlrev_b32_e32 v18, 16, v137
	v_and_b32_e32 v19, 0xffff0000, v137
	v_pk_fma_f32 v[36:37], v[140:141], v[36:37], v[16:17]
	v_pk_fma_f32 v[38:39], v[140:141], v[38:39], v[18:19]
	v_lshlrev_b32_e32 v16, 16, v138
	v_and_b32_e32 v17, 0xffff0000, v138
	v_lshlrev_b32_e32 v18, 16, v139
	v_and_b32_e32 v19, 0xffff0000, v139
	v_pk_fma_f32 v[40:41], v[140:141], v[40:41], v[16:17]
	v_pk_fma_f32 v[42:43], v[140:141], v[42:43], v[18:19]
	s_lshl_b32 s38, s32, 6
	s_mul_i32 s38, s38, s18
	s_add_i32 s38, s38, s76
	s_cmp_eq_u32 s11, 6
	s_cbranch_scc1 .Lm20_s0_den
	s_mul_i32 s39, s38, 0x300
	v_add_u32_e32 v15, s39, v7
	v_cvt_pk_bf16_f32 v56, v56, v57
	v_cvt_pk_bf16_f32 v57, v58, v59
	global_store_dwordx2 v15, v[56:57], s[78:79]
	s_add_i32 s38, s38, s77
	s_mul_i32 s39, s38, 0x300
	v_add_u32_e32 v15, s39, v7
	v_cvt_pk_bf16_f32 v60, v60, v61
	v_cvt_pk_bf16_f32 v61, v62, v63
	global_store_dwordx2 v15, v[60:61], s[78:79]
	s_add_i32 s38, s38, s77
	s_mul_i32 s39, s38, 0x300
	v_add_u32_e32 v15, s39, v7
	v_cvt_pk_bf16_f32 v64, v64, v65
	v_cvt_pk_bf16_f32 v65, v66, v67
	global_store_dwordx2 v15, v[64:65], s[78:79]
	s_add_i32 s38, s38, s77
	s_mul_i32 s39, s38, 0x300
	v_add_u32_e32 v15, s39, v7
	v_cvt_pk_bf16_f32 v68, v68, v69
	v_cvt_pk_bf16_f32 v69, v70, v71
	global_store_dwordx2 v15, v[68:69], s[78:79]
	s_branch .Lm20_s0_od
; DI unsigned cvtpk(float lo, float hi) { const f2_t v = {lo, hi}; return __builtin_bit_cast(unsigned, __builtin_convertvector(v, bf2_t)); }
; DI void m2_step(const M2Small& o, const LAS unsigned char* slot, f32x4 (&C)[6], bf16* num, float* den, int dir, int b, int hh, int nt, int c, int lane, int fr, int qd) {
;     ...
;     for (int i = 0; i < 3; ++i) { sB[i].u[0] = cvtpk(C[2 * i][0], C[2 * i][1]); sB[i].u[1] = cvtpk(C[2 * i][2], C[2 * i][3]); sB[i].u[2] = cvtpk(C[2 * i + 1][0], C[2 * i + 1][1]); sB[i].u[3] = cvtpk(C[2 * i + 1][2], C[2 * i + 1][3]); }
;     ...
;           if (nt < 6) { u32x2_t w; w.x = cvtpk(acc[0], acc[1]); w.y = cvtpk(acc[2], acc[3]); *(u32x2_t*)(num + ((size_t)dir * NT + tok) * MW + hh * 96 + 16 * nt + 4 * qd) = w; }
;           else if (qd == 0) den[((size_t)dir * NT + tok) * 4 + hh] = acc[0]; } }
.Lm20_s0_den:
	s_mov_b64 exec, s[74:75]
	s_lshl_b32 s39, s38, 4
	v_add_u32_e32 v15, s39, v8
	global_store_dword v15, v56, s[80:81]
	s_add_i32 s38, s38, s77
	s_lshl_b32 s39, s38, 4
	v_add_u32_e32 v15, s39, v8
	global_store_dword v15, v60, s[80:81]
	s_add_i32 s38, s38, s77
	s_lshl_b32 s39, s38, 4
	v_add_u32_e32 v15, s39, v8
	global_store_dword v15, v64, s[80:81]
	s_add_i32 s38, s38, s77
	s_lshl_b32 s39, s38, 4
	v_add_u32_e32 v15, s39, v8
	global_store_dword v15, v68, s[80:81]
	s_mov_b64 exec, -1
.Lm20_s0_od:
	s_add_i32 s30, s32, 4
	s_cmpk_lt_u32 s30, 0x20
	s_cbranch_scc0 .Lm20_s0_nold
	s_mul_i32 s27, s30, 0xbd00
	s_add_u32 s28, s14, s27
	s_addc_u32 s29, s15, 0
	global_load_dwordx2 v[120:121], v4, s[28:29] nt
	global_load_dwordx2 v[122:123], v4, s[28:29] offset:512 nt
	global_load_dwordx2 v[124:125], v4, s[28:29] offset:1024 nt
	global_load_dwordx2 v[126:127], v4, s[28:29] offset:1536 nt
	global_load_dwordx2 v[128:129], v5, s[28:29] nt
	global_load_dwordx2 v[130:131], v5, s[28:29] offset:512 nt
	global_load_dwordx2 v[132:133], v5, s[28:29] offset:1024 nt
	global_load_dwordx2 v[134:135], v5, s[28:29] offset:1536 nt
	global_load_dwordx2 v[136:137], v5, s[28:29] offset:2048 nt
	global_load_dwordx2 v[138:139], v5, s[28:29] offset:2560 nt
	global_load_dword v140, v6, s[28:29]
.Lm20_s0_nold:
	s_add_i32 s32, s31, 1
	s_add_i32 s33, s32, 1
	s_and_b32 s34, s32, 7
	s_mul_i32 s35, s34, 0x3000
	v_cvt_pk_bf16_f32 v44, v20, v21
	v_cvt_pk_bf16_f32 v45, v22, v23
	v_cvt_pk_bf16_f32 v46, v24, v25
	v_cvt_pk_bf16_f32 v47, v26, v27
	v_cvt_pk_bf16_f32 v48, v28, v29
	v_cvt_pk_bf16_f32 v49, v30, v31
	v_cvt_pk_bf16_f32 v50, v32, v33
	v_cvt_pk_bf16_f32 v51, v34, v35
	v_cvt_pk_bf16_f32 v52, v36, v37
	v_cvt_pk_bf16_f32 v53, v38, v39
	v_cvt_pk_bf16_f32 v54, v40, v41
	v_cvt_pk_bf16_f32 v55, v42, v43
	s_waitcnt lgkmcnt(0)
	v_cmp_eq_u32_e32 vcc, s33, v11
	s_cbranch_vccnz .Lm20_s1_rdy
	s_mov_b32 s36, 0x400000

.Lm20_w1_first:
	s_waitcnt vmcnt(37)
	s_branch .Lm20_w1_done

; #define LAS __attribute__((address_space(3)))
; DI unsigned cvtpk(float lo, float hi) { const f2_t v = {lo, hi}; return __builtin_bit_cast(unsigned, __builtin_convertvector(v, bf2_t)); }
; #define MFMA16(a, b, c) __builtin_amdgcn_mfma_f32_16x16x32_bf16((a), (b), (c), 0, 0, 0)
; DI f32x4 unpk4(const u32x2_t w) { return (f32x4){__uint_as_float(w.x << 16), __uint_as_float(w.x & 0xffff0000u), __uint_as_float(w.y << 16), __uint_as_float(w.y & 0xffff0000u)}; }
; DI void m2_step(const M2Small& o, const LAS unsigned char* slot, f32x4 (&C)[6], bf16* num, float* den, int dir, int b, int hh, int nt, int c, int lane, int fr, int qd) {
;     union { unsigned u[4]; bf16x8_t v; } sB[3];
; #pragma unroll
;     for (int i = 0; i < 3; ++i) { sB[i].u[0] = cvtpk(C[2 * i][0], C[2 * i][1]); sB[i].u[1] = cvtpk(C[2 * i][2], C[2 * i][3]); sB[i].u[2] = cvtpk(C[2 * i + 1][0], C[2 * i + 1][1]); sB[i].u[3] = cvtpk(C[2 * i + 1][2], C[2 * i + 1][3]); }
; #pragma unroll
;     for (int jt = 0; jt < 4; ++jt) { f32x4 acc = unpk4(o.ni[jt]);
; #pragma unroll
;         for (int i = 0; i < 3; ++i) { const bf16x8_t qf = *(const LAS bf16x8_t*)(slot + (3 * jt + i) * 1024 + lane * 16); acc = MFMA16(sB[i].v, qf, acc); }
;         { const int jj = 16 * jt + fr; const int tt = dir ? SEQ - 1 - (c * 64 + jj) : c * 64 + jj; const size_t tok = (size_t)b * SEQ + tt;
;           if (nt < 6) { u32x2_t w; w.x = cvtpk(acc[0], acc[1]); w.y = cvtpk(acc[2], acc[3]); *(u32x2_t*)(num + ((size_t)dir * NT + tok) * MW + hh * 96 + 16 * nt + 4 * qd) = w; }
;           else if (qd == 0) den[((size_t)dir * NT + tok) * 4 + hh] = acc[0]; } }
; #pragma unroll
;     for (int kt = 0; kt < 6; ++kt) C[kt] = C[kt] * o.dec + unpk4(o.uu[kt]);
.Lm20_w1_done:
	v_lshlrev_b32_e32 v56, 16, v148
	v_and_b32_e32 v57, 0xffff0000, v148
	v_lshlrev_b32_e32 v58, 16, v149
	v_and_b32_e32 v59, 0xffff0000, v149
	v_lshlrev_b32_e32 v60, 16, v150
	v_and_b32_e32 v61, 0xffff0000, v150
	v_lshlrev_b32_e32 v62, 16, v151
	v_and_b32_e32 v63, 0xffff0000, v151
	v_lshlrev_b32_e32 v64, 16, v152
	v_and_b32_e32 v65, 0xffff0000, v152
	v_lshlrev_b32_e32 v66, 16, v153
	v_and_b32_e32 v67, 0xffff0000, v153
	v_lshlrev_b32_e32 v68, 16, v154
	v_and_b32_e32 v69, 0xffff0000, v154
	v_lshlrev_b32_e32 v70, 16, v155
	v_and_b32_e32 v71, 0xffff0000, v155
	s_waitcnt lgkmcnt(11)
	v_mfma_f32_16x16x32_bf16 v[56:59], v[44:47], v[72:75], v[56:59]
	s_waitcnt lgkmcnt(10)
	v_mfma_f32_16x16x32_bf16 v[60:63], v[44:47], v[76:79], v[60:63]
	s_waitcnt lgkmcnt(9)
	v_mfma_f32_16x16x32_bf16 v[64:67], v[44:47], v[80:83], v[64:67]
	s_waitcnt lgkmcnt(8)
	v_mfma_f32_16x16x32_bf16 v[68:71], v[44:47], v[84:87], v[68:71]
	s_add_i32 s37, s32, 1
	s_and_b32 s37, s37, 7
	s_lshl_b32 s37, s37, 2
	s_add_i32 s37, s37, 0x18000
	v_mov_b32_e32 v10, s37
	s_waitcnt lgkmcnt(7)
	v_mfma_f32_16x16x32_bf16 v[56:59], v[48:51], v[88:91], v[56:59]
	s_waitcnt lgkmcnt(6)
	v_mfma_f32_16x16x32_bf16 v[60:63], v[48:51], v[92:95], v[60:63]
	s_waitcnt lgkmcnt(5)
	v_mfma_f32_16x16x32_bf16 v[64:67], v[48:51], v[96:99], v[64:67]
	s_waitcnt lgkmcnt(4)
	v_mfma_f32_16x16x32_bf16 v[68:71], v[48:51], v[100:103], v[68:71]
	s_waitcnt lgkmcnt(3)
	v_mfma_f32_16x16x32_bf16 v[56:59], v[52:55], v[104:107], v[56:59]
	s_waitcnt lgkmcnt(2)
	v_mfma_f32_16x16x32_bf16 v[60:63], v[52:55], v[108:111], v[60:63]
	s_waitcnt lgkmcnt(1)
	v_mfma_f32_16x16x32_bf16 v[64:67], v[52:55], v[112:115], v[64:67]
	s_waitcnt lgkmcnt(0)
	v_mfma_f32_16x16x32_bf16 v[68:71], v[52:55], v[116:119], v[68:71]
	s_mov_b64 exec, s[72:73]
	v_mov_b32_e32 v13, s82
	v_mov_b32_e32 v14, s33
	ds_write_b32 v13, v14
	s_mov_b64 exec, -1
	ds_read_b32 v11, v10
	v_mov_b32_e32 v169, v168
	v_lshlrev_b32_e32 v16, 16, v156
	v_and_b32_e32 v17, 0xffff0000, v156
	v_lshlrev_b32_e32 v18, 16, v157
	v_and_b32_e32 v19, 0xffff0000, v157
	v_pk_fma_f32 v[20:21], v[168:169], v[20:21], v[16:17]
	v_pk_fma_f32 v[22:23], v[168:169], v[22:23], v[18:19]
	v_lshlrev_b32_e32 v16, 16, v158
	v_and_b32_e32 v17, 0xffff0000, v158
	v_lshlrev_b32_e32 v18, 16, v159
	v_and_b32_e32 v19, 0xffff0000, v159
	v_pk_fma_f32 v[24:25], v[168:169], v[24:25], v[16:17]
	v_pk_fma_f32 v[26:27], v[168:169], v[26:27], v[18:19]
	v_lshlrev_b32_e32 v16, 16, v160
	v_and_b32_e32 v17, 0xffff0000, v160
	v_lshlrev_b32_e32 v18, 16, v161
	v_and_b32_e32 v19, 0xffff0000, v161
	v_pk_fma_f32 v[28:29], v[168:169], v[28:29], v[16:17]
	v_pk_fma_f32 v[30:31], v[168:169], v[30:31], v[18:19]
	v_lshlrev_b32_e32 v16, 16, v162
	v_and_b32_e32 v17, 0xffff0000, v162
	v_lshlrev_b32_e32 v18, 16, v163
	v_and_b32_e32 v19, 0xffff0000, v163
	v_pk_fma_f32 v[32:33], v[168:169], v[32:33], v[16:17]
	v_pk_fma_f32 v[34:35], v[168:169], v[34:35], v[18:19]
	v_lshlrev_b32_e32 v16, 16, v164
	v_and_b32_e32 v17, 0xffff0000, v164
	v_lshlrev_b32_e32 v18, 16, v165
	v_and_b32_e32 v19, 0xffff0000, v165
	v_pk_fma_f32 v[36:37], v[168:169], v[36:37], v[16:17]
	v_pk_fma_f32 v[38:39], v[168:169], v[38:39], v[18:19]
	v_lshlrev_b32_e32 v16, 16, v166
	v_and_b32_e32 v17, 0xffff0000, v166
	v_lshlrev_b32_e32 v18, 16, v167
	v_and_b32_e32 v19, 0xffff0000, v167
	v_pk_fma_f32 v[40:41], v[168:169], v[40:41], v[16:17]
	v_pk_fma_f32 v[42:43], v[168:169], v[42:43], v[18:19]
	s_lshl_b32 s38, s32, 6
	s_mul_i32 s38, s38, s18
	s_add_i32 s38, s38, s76
	s_cmp_eq_u32 s11, 6
	s_cbranch_scc1 .Lm20_s1_den
	s_mul_i32 s39, s38, 0x300
	v_add_u32_e32 v15, s39, v7
	v_cvt_pk_bf16_f32 v56, v56, v57
	v_cvt_pk_bf16_f32 v57, v58, v59
	global_store_dwordx2 v15, v[56:57], s[78:79]
	s_add_i32 s38, s38, s77
	s_mul_i32 s39, s38, 0x300
	v_add_u32_e32 v15, s39, v7
	v_cvt_pk_bf16_f32 v60, v60, v61
	v_cvt_pk_bf16_f32 v61, v62, v63
	global_store_dwordx2 v15, v[60:61], s[78:79]
	s_add_i32 s38, s38, s77
	s_mul_i32 s39, s38, 0x300
	v_add_u32_e32 v15, s39, v7
	v_cvt_pk_bf16_f32 v64, v64, v65
	v_cvt_pk_bf16_f32 v65, v66, v67
	global_store_dwordx2 v15, v[64:65], s[78:79]
	s_add_i32 s38, s38, s77
	s_mul_i32 s39, s38, 0x300
	v_add_u32_e32 v15, s39, v7
	v_cvt_pk_bf16_f32 v68, v68, v69
	v_cvt_pk_bf16_f32 v69, v70, v71
	global_store_dwordx2 v15, v[68:69], s[78:79]
	s_branch .Lm20_s1_od

; DI unsigned cvtpk(float lo, float hi) { const f2_t v = {lo, hi}; return __builtin_bit_cast(unsigned, __builtin_convertvector(v, bf2_t)); }
; DI void m2_step(const M2Small& o, const LAS unsigned char* slot, f32x4 (&C)[6], bf16* num, float* den, int dir, int b, int hh, int nt, int c, int lane, int fr, int qd) {
;     ...
;     for (int i = 0; i < 3; ++i) { sB[i].u[0] = cvtpk(C[2 * i][0], C[2 * i][1]); sB[i].u[1] = cvtpk(C[2 * i][2], C[2 * i][3]); sB[i].u[2] = cvtpk(C[2 * i + 1][0], C[2 * i + 1][1]); sB[i].u[3] = cvtpk(C[2 * i + 1][2], C[2 * i + 1][3]); }
.Lm20_s1_od:
	s_add_i32 s30, s32, 4
	s_cmpk_lt_u32 s30, 0x20
	s_cbranch_scc0 .Lm20_s1_nold
	s_mul_i32 s27, s30, 0xbd00
	s_add_u32 s28, s14, s27
	s_addc_u32 s29, s15, 0
	global_load_dwordx2 v[148:149], v4, s[28:29] nt
	global_load_dwordx2 v[150:151], v4, s[28:29] offset:512 nt
	global_load_dwordx2 v[152:153], v4, s[28:29] offset:1024 nt
	global_load_dwordx2 v[154:155], v4, s[28:29] offset:1536 nt
	global_load_dwordx2 v[156:157], v5, s[28:29] nt
	global_load_dwordx2 v[158:159], v5, s[28:29] offset:512 nt
	global_load_dwordx2 v[160:161], v5, s[28:29] offset:1024 nt
	global_load_dwordx2 v[162:163], v5, s[28:29] offset:1536 nt
	global_load_dwordx2 v[164:165], v5, s[28:29] offset:2048 nt
	global_load_dwordx2 v[166:167], v5, s[28:29] offset:2560 nt
	global_load_dword v168, v6, s[28:29]
.Lm20_s1_nold:
	s_add_i32 s32, s31, 2
	s_add_i32 s33, s32, 1
	s_and_b32 s34, s32, 7
	s_mul_i32 s35, s34, 0x3000
	v_cvt_pk_bf16_f32 v44, v20, v21
	v_cvt_pk_bf16_f32 v45, v22, v23
	v_cvt_pk_bf16_f32 v46, v24, v25
	v_cvt_pk_bf16_f32 v47, v26, v27
	v_cvt_pk_bf16_f32 v48, v28, v29
	v_cvt_pk_bf16_f32 v49, v30, v31
	v_cvt_pk_bf16_f32 v50, v32, v33
	v_cvt_pk_bf16_f32 v51, v34, v35
	v_cvt_pk_bf16_f32 v52, v36, v37
	v_cvt_pk_bf16_f32 v53, v38, v39
	v_cvt_pk_bf16_f32 v54, v40, v41
	v_cvt_pk_bf16_f32 v55, v42, v43
	s_waitcnt lgkmcnt(0)
	v_cmp_eq_u32_e32 vcc, s33, v11
	s_cbranch_vccnz .Lm20_s2_rdy
	s_mov_b32 s36, 0x400000

.Lm20_w2_first:
	s_waitcnt vmcnt(41)
	s_branch .Lm20_w2_done

; #define LAS __attribute__((address_space(3)))
; DI unsigned cvtpk(float lo, float hi) { const f2_t v = {lo, hi}; return __builtin_bit_cast(unsigned, __builtin_convertvector(v, bf2_t)); }
; #define MFMA16(a, b, c) __builtin_amdgcn_mfma_f32_16x16x32_bf16((a), (b), (c), 0, 0, 0)
; DI f32x4 unpk4(const u32x2_t w) { return (f32x4){__uint_as_float(w.x << 16), __uint_as_float(w.x & 0xffff0000u), __uint_as_float(w.y << 16), __uint_as_float(w.y & 0xffff0000u)}; }
; DI void m2_step(const M2Small& o, const LAS unsigned char* slot, f32x4 (&C)[6], bf16* num, float* den, int dir, int b, int hh, int nt, int c, int lane, int fr, int qd) {
;     union { unsigned u[4]; bf16x8_t v; } sB[3];
; #pragma unroll
;     for (int i = 0; i < 3; ++i) { sB[i].u[0] = cvtpk(C[2 * i][0], C[2 * i][1]); sB[i].u[1] = cvtpk(C[2 * i][2], C[2 * i][3]); sB[i].u[2] = cvtpk(C[2 * i + 1][0], C[2 * i + 1][1]); sB[i].u[3] = cvtpk(C[2 * i + 1][2], C[2 * i + 1][3]); }
; #pragma unroll
;     for (int jt = 0; jt < 4; ++jt) { f32x4 acc = unpk4(o.ni[jt]);
; #pragma unroll
;         for (int i = 0; i < 3; ++i) { const bf16x8_t qf = *(const LAS bf16x8_t*)(slot + (3 * jt + i) * 1024 + lane * 16); acc = MFMA16(sB[i].v, qf, acc); }
;         { const int jj = 16 * jt + fr; const int tt = dir ? SEQ - 1 - (c * 64 + jj) : c * 64 + jj; const size_t tok = (size_t)b * SEQ + tt;
;           if (nt < 6) { u32x2_t w; w.x = cvtpk(acc[0], acc[1]); w.y = cvtpk(acc[2], acc[3]); *(u32x2_t*)(num + ((size_t)dir * NT + tok) * MW + hh * 96 + 16 * nt + 4 * qd) = w; }
;           else if (qd == 0) den[((size_t)dir * NT + tok) * 4 + hh] = acc[0]; } }
; #pragma unroll
;     for (int kt = 0; kt < 6; ++kt) C[kt] = C[kt] * o.dec + unpk4(o.uu[kt]);
.Lm20_w2_done:
	v_lshlrev_b32_e32 v56, 16, v172
	v_and_b32_e32 v57, 0xffff0000, v172
	v_lshlrev_b32_e32 v58, 16, v173
	v_and_b32_e32 v59, 0xffff0000, v173
	v_lshlrev_b32_e32 v60, 16, v174
	v_and_b32_e32 v61, 0xffff0000, v174
	v_lshlrev_b32_e32 v62, 16, v175
	v_and_b32_e32 v63, 0xffff0000, v175
	v_lshlrev_b32_e32 v64, 16, v176
	v_and_b32_e32 v65, 0xffff0000, v176
	v_lshlrev_b32_e32 v66, 16, v177
	v_and_b32_e32 v67, 0xffff0000, v177
	v_lshlrev_b32_e32 v68, 16, v178
	v_and_b32_e32 v69, 0xffff0000, v178
	v_lshlrev_b32_e32 v70, 16, v179
	v_and_b32_e32 v71, 0xffff0000, v179
	s_waitcnt lgkmcnt(11)
	v_mfma_f32_16x16x32_bf16 v[56:59], v[44:47], v[72:75], v[56:59]
	s_waitcnt lgkmcnt(10)
	v_mfma_f32_16x16x32_bf16 v[60:63], v[44:47], v[76:79], v[60:63]
	s_waitcnt lgkmcnt(9)
	v_mfma_f32_16x16x32_bf16 v[64:67], v[44:47], v[80:83], v[64:67]
	s_waitcnt lgkmcnt(8)
	v_mfma_f32_16x16x32_bf16 v[68:71], v[44:47], v[84:87], v[68:71]
	s_add_i32 s37, s32, 1
	s_and_b32 s37, s37, 7
	s_lshl_b32 s37, s37, 2
	s_add_i32 s37, s37, 0x18000
	v_mov_b32_e32 v10, s37
	s_waitcnt lgkmcnt(7)
	v_mfma_f32_16x16x32_bf16 v[56:59], v[48:51], v[88:91], v[56:59]
	s_waitcnt lgkmcnt(6)
	v_mfma_f32_16x16x32_bf16 v[60:63], v[48:51], v[92:95], v[60:63]
	s_waitcnt lgkmcnt(5)
	v_mfma_f32_16x16x32_bf16 v[64:67], v[48:51], v[96:99], v[64:67]
	s_waitcnt lgkmcnt(4)
	v_mfma_f32_16x16x32_bf16 v[68:71], v[48:51], v[100:103], v[68:71]
	s_waitcnt lgkmcnt(3)
	v_mfma_f32_16x16x32_bf16 v[56:59], v[52:55], v[104:107], v[56:59]
	s_waitcnt lgkmcnt(2)
	v_mfma_f32_16x16x32_bf16 v[60:63], v[52:55], v[108:111], v[60:63]
	s_waitcnt lgkmcnt(1)
	v_mfma_f32_16x16x32_bf16 v[64:67], v[52:55], v[112:115], v[64:67]
	s_waitcnt lgkmcnt(0)
	v_mfma_f32_16x16x32_bf16 v[68:71], v[52:55], v[116:119], v[68:71]
	s_mov_b64 exec, s[72:73]
	v_mov_b32_e32 v13, s82
	v_mov_b32_e32 v14, s33
	ds_write_b32 v13, v14
	s_mov_b64 exec, -1
	ds_read_b32 v11, v10
	v_mov_b32_e32 v193, v192
	v_lshlrev_b32_e32 v16, 16, v180
	v_and_b32_e32 v17, 0xffff0000, v180
	v_lshlrev_b32_e32 v18, 16, v181
	v_and_b32_e32 v19, 0xffff0000, v181
	v_pk_fma_f32 v[20:21], v[192:193], v[20:21], v[16:17]
	v_pk_fma_f32 v[22:23], v[192:193], v[22:23], v[18:19]
	v_lshlrev_b32_e32 v16, 16, v182
	v_and_b32_e32 v17, 0xffff0000, v182
	v_lshlrev_b32_e32 v18, 16, v183
	v_and_b32_e32 v19, 0xffff0000, v183
	v_pk_fma_f32 v[24:25], v[192:193], v[24:25], v[16:17]
	v_pk_fma_f32 v[26:27], v[192:193], v[26:27], v[18:19]
	v_lshlrev_b32_e32 v16, 16, v184
	v_and_b32_e32 v17, 0xffff0000, v184
	v_lshlrev_b32_e32 v18, 16, v185
	v_and_b32_e32 v19, 0xffff0000, v185
	v_pk_fma_f32 v[28:29], v[192:193], v[28:29], v[16:17]
	v_pk_fma_f32 v[30:31], v[192:193], v[30:31], v[18:19]
	v_lshlrev_b32_e32 v16, 16, v186
	v_and_b32_e32 v17, 0xffff0000, v186
	v_lshlrev_b32_e32 v18, 16, v187
	v_and_b32_e32 v19, 0xffff0000, v187
	v_pk_fma_f32 v[32:33], v[192:193], v[32:33], v[16:17]
	v_pk_fma_f32 v[34:35], v[192:193], v[34:35], v[18:19]
	v_lshlrev_b32_e32 v16, 16, v188
	v_and_b32_e32 v17, 0xffff0000, v188
	v_lshlrev_b32_e32 v18, 16, v189
	v_and_b32_e32 v19, 0xffff0000, v189
	v_pk_fma_f32 v[36:37], v[192:193], v[36:37], v[16:17]
	v_pk_fma_f32 v[38:39], v[192:193], v[38:39], v[18:19]
	v_lshlrev_b32_e32 v16, 16, v190
	v_and_b32_e32 v17, 0xffff0000, v190
	v_lshlrev_b32_e32 v18, 16, v191
	v_and_b32_e32 v19, 0xffff0000, v191
	v_pk_fma_f32 v[40:41], v[192:193], v[40:41], v[16:17]
	v_pk_fma_f32 v[42:43], v[192:193], v[42:43], v[18:19]
	s_lshl_b32 s38, s32, 6
	s_mul_i32 s38, s38, s18
	s_add_i32 s38, s38, s76
	s_cmp_eq_u32 s11, 6
	s_cbranch_scc1 .Lm20_s2_den
	s_mul_i32 s39, s38, 0x300
	v_add_u32_e32 v15, s39, v7
	v_cvt_pk_bf16_f32 v56, v56, v57
	v_cvt_pk_bf16_f32 v57, v58, v59
	global_store_dwordx2 v15, v[56:57], s[78:79]
	s_add_i32 s38, s38, s77
	s_mul_i32 s39, s38, 0x300
	v_add_u32_e32 v15, s39, v7
	v_cvt_pk_bf16_f32 v60, v60, v61
	v_cvt_pk_bf16_f32 v61, v62, v63
	global_store_dwordx2 v15, v[60:61], s[78:79]
	s_add_i32 s38, s38, s77
	s_mul_i32 s39, s38, 0x300
	v_add_u32_e32 v15, s39, v7
	v_cvt_pk_bf16_f32 v64, v64, v65
	v_cvt_pk_bf16_f32 v65, v66, v67
	global_store_dwordx2 v15, v[64:65], s[78:79]
	s_add_i32 s38, s38, s77
	s_mul_i32 s39, s38, 0x300
	v_add_u32_e32 v15, s39, v7
	v_cvt_pk_bf16_f32 v68, v68, v69
	v_cvt_pk_bf16_f32 v69, v70, v71
	global_store_dwordx2 v15, v[68:69], s[78:79]
	s_branch .Lm20_s2_od

; DI unsigned cvtpk(float lo, float hi) { const f2_t v = {lo, hi}; return __builtin_bit_cast(unsigned, __builtin_convertvector(v, bf2_t)); }
; DI void m2_step(const M2Small& o, const LAS unsigned char* slot, f32x4 (&C)[6], bf16* num, float* den, int dir, int b, int hh, int nt, int c, int lane, int fr, int qd) {
;     ...
;     for (int i = 0; i < 3; ++i) { sB[i].u[0] = cvtpk(C[2 * i][0], C[2 * i][1]); sB[i].u[1] = cvtpk(C[2 * i][2], C[2 * i][3]); sB[i].u[2] = cvtpk(C[2 * i + 1][0], C[2 * i + 1][1]); sB[i].u[3] = cvtpk(C[2 * i + 1][2], C[2 * i + 1][3]); }
.Lm20_s2_od:
	s_add_i32 s30, s32, 4
	s_cmpk_lt_u32 s30, 0x20
	s_cbranch_scc0 .Lm20_s2_nold
	s_mul_i32 s27, s30, 0xbd00
	s_add_u32 s28, s14, s27
	s_addc_u32 s29, s15, 0
	global_load_dwordx2 v[172:173], v4, s[28:29] nt
	global_load_dwordx2 v[174:175], v4, s[28:29] offset:512 nt
	global_load_dwordx2 v[176:177], v4, s[28:29] offset:1024 nt
	global_load_dwordx2 v[178:179], v4, s[28:29] offset:1536 nt
	global_load_dwordx2 v[180:181], v5, s[28:29] nt
	global_load_dwordx2 v[182:183], v5, s[28:29] offset:512 nt
	global_load_dwordx2 v[184:185], v5, s[28:29] offset:1024 nt
	global_load_dwordx2 v[186:187], v5, s[28:29] offset:1536 nt
	global_load_dwordx2 v[188:189], v5, s[28:29] offset:2048 nt
	global_load_dwordx2 v[190:191], v5, s[28:29] offset:2560 nt
	global_load_dword v192, v6, s[28:29]
.Lm20_s2_nold:
	s_add_i32 s32, s31, 3
	s_add_i32 s33, s32, 1
	s_and_b32 s34, s32, 7
	s_mul_i32 s35, s34, 0x3000
	v_cvt_pk_bf16_f32 v44, v20, v21
	v_cvt_pk_bf16_f32 v45, v22, v23
	v_cvt_pk_bf16_f32 v46, v24, v25
	v_cvt_pk_bf16_f32 v47, v26, v27
	v_cvt_pk_bf16_f32 v48, v28, v29
	v_cvt_pk_bf16_f32 v49, v30, v31
	v_cvt_pk_bf16_f32 v50, v32, v33
	v_cvt_pk_bf16_f32 v51, v34, v35
	v_cvt_pk_bf16_f32 v52, v36, v37
	v_cvt_pk_bf16_f32 v53, v38, v39
	v_cvt_pk_bf16_f32 v54, v40, v41
	v_cvt_pk_bf16_f32 v55, v42, v43
	s_waitcnt lgkmcnt(0)
	v_cmp_eq_u32_e32 vcc, s33, v11
	s_cbranch_vccnz .Lm20_s3_rdy
	s_mov_b32 s36, 0x400000

.Lm20_w3_first:
	s_waitcnt vmcnt(45)
	s_branch .Lm20_w3_done

; #define LAS __attribute__((address_space(3)))
; DI unsigned cvtpk(float lo, float hi) { const f2_t v = {lo, hi}; return __builtin_bit_cast(unsigned, __builtin_convertvector(v, bf2_t)); }
; #define MFMA16(a, b, c) __builtin_amdgcn_mfma_f32_16x16x32_bf16((a), (b), (c), 0, 0, 0)
; DI f32x4 unpk4(const u32x2_t w) { return (f32x4){__uint_as_float(w.x << 16), __uint_as_float(w.x & 0xffff0000u), __uint_as_float(w.y << 16), __uint_as_float(w.y & 0xffff0000u)}; }
; DI void m2_step(const M2Small& o, const LAS unsigned char* slot, f32x4 (&C)[6], bf16* num, float* den, int dir, int b, int hh, int nt, int c, int lane, int fr, int qd) {
;     union { unsigned u[4]; bf16x8_t v; } sB[3];
; #pragma unroll
;     for (int i = 0; i < 3; ++i) { sB[i].u[0] = cvtpk(C[2 * i][0], C[2 * i][1]); sB[i].u[1] = cvtpk(C[2 * i][2], C[2 * i][3]); sB[i].u[2] = cvtpk(C[2 * i + 1][0], C[2 * i + 1][1]); sB[i].u[3] = cvtpk(C[2 * i + 1][2], C[2 * i + 1][3]); }
; #pragma unroll
;     for (int jt = 0; jt < 4; ++jt) { f32x4 acc = unpk4(o.ni[jt]);
; #pragma unroll
;         for (int i = 0; i < 3; ++i) { const bf16x8_t qf = *(const LAS bf16x8_t*)(slot + (3 * jt + i) * 1024 + lane * 16); acc = MFMA16(sB[i].v, qf, acc); }
;         { const int jj = 16 * jt + fr; const int tt = dir ? SEQ - 1 - (c * 64 + jj) : c * 64 + jj; const size_t tok = (size_t)b * SEQ + tt;
;           if (nt < 6) { u32x2_t w; w.x = cvtpk(acc[0], acc[1]); w.y = cvtpk(acc[2], acc[3]); *(u32x2_t*)(num + ((size_t)dir * NT + tok) * MW + hh * 96 + 16 * nt + 4 * qd) = w; }
;           else if (qd == 0) den[((size_t)dir * NT + tok) * 4 + hh] = acc[0]; } }
; #pragma unroll
;     for (int kt = 0; kt < 6; ++kt) C[kt] = C[kt] * o.dec + unpk4(o.uu[kt]);
.Lm20_w3_done:
	v_lshlrev_b32_e32 v56, 16, v194
	v_and_b32_e32 v57, 0xffff0000, v194
	v_lshlrev_b32_e32 v58, 16, v195
	v_and_b32_e32 v59, 0xffff0000, v195
	v_lshlrev_b32_e32 v60, 16, v196
	v_and_b32_e32 v61, 0xffff0000, v196
	v_lshlrev_b32_e32 v62, 16, v197
	v_and_b32_e32 v63, 0xffff0000, v197
	v_lshlrev_b32_e32 v64, 16, v198
	v_and_b32_e32 v65, 0xffff0000, v198
	v_lshlrev_b32_e32 v66, 16, v199
	v_and_b32_e32 v67, 0xffff0000, v199
	v_lshlrev_b32_e32 v68, 16, v200
	v_and_b32_e32 v69, 0xffff0000, v200
	v_lshlrev_b32_e32 v70, 16, v201
	v_and_b32_e32 v71, 0xffff0000, v201
	s_waitcnt lgkmcnt(11)
	v_mfma_f32_16x16x32_bf16 v[56:59], v[44:47], v[72:75], v[56:59]
	s_waitcnt lgkmcnt(10)
	v_mfma_f32_16x16x32_bf16 v[60:63], v[44:47], v[76:79], v[60:63]
	s_waitcnt lgkmcnt(9)
	v_mfma_f32_16x16x32_bf16 v[64:67], v[44:47], v[80:83], v[64:67]
	s_waitcnt lgkmcnt(8)
	v_mfma_f32_16x16x32_bf16 v[68:71], v[44:47], v[84:87], v[68:71]
	s_add_i32 s37, s32, 1
	s_and_b32 s37, s37, 7
	s_lshl_b32 s37, s37, 2
	s_add_i32 s37, s37, 0x18000
	v_mov_b32_e32 v10, s37
	s_waitcnt lgkmcnt(7)
	v_mfma_f32_16x16x32_bf16 v[56:59], v[48:51], v[88:91], v[56:59]
	s_waitcnt lgkmcnt(6)
	v_mfma_f32_16x16x32_bf16 v[60:63], v[48:51], v[92:95], v[60:63]
	s_waitcnt lgkmcnt(5)
	v_mfma_f32_16x16x32_bf16 v[64:67], v[48:51], v[96:99], v[64:67]
	s_waitcnt lgkmcnt(4)
	v_mfma_f32_16x16x32_bf16 v[68:71], v[48:51], v[100:103], v[68:71]
	s_waitcnt lgkmcnt(3)
	v_mfma_f32_16x16x32_bf16 v[56:59], v[52:55], v[104:107], v[56:59]
	s_waitcnt lgkmcnt(2)
	v_mfma_f32_16x16x32_bf16 v[60:63], v[52:55], v[108:111], v[60:63]
	s_waitcnt lgkmcnt(1)
	v_mfma_f32_16x16x32_bf16 v[64:67], v[52:55], v[112:115], v[64:67]
	s_waitcnt lgkmcnt(0)
	v_mfma_f32_16x16x32_bf16 v[68:71], v[52:55], v[116:119], v[68:71]
	s_mov_b64 exec, s[72:73]
	v_mov_b32_e32 v13, s82
	v_mov_b32_e32 v14, s33
	ds_write_b32 v13, v14
	s_mov_b64 exec, -1
	ds_read_b32 v11, v10
	v_mov_b32_e32 v215, v214
	v_lshlrev_b32_e32 v16, 16, v202
	v_and_b32_e32 v17, 0xffff0000, v202
	v_lshlrev_b32_e32 v18, 16, v203
	v_and_b32_e32 v19, 0xffff0000, v203
	v_pk_fma_f32 v[20:21], v[214:215], v[20:21], v[16:17]
	v_pk_fma_f32 v[22:23], v[214:215], v[22:23], v[18:19]
	v_lshlrev_b32_e32 v16, 16, v204
	v_and_b32_e32 v17, 0xffff0000, v204
	v_lshlrev_b32_e32 v18, 16, v205
	v_and_b32_e32 v19, 0xffff0000, v205
	v_pk_fma_f32 v[24:25], v[214:215], v[24:25], v[16:17]
	v_pk_fma_f32 v[26:27], v[214:215], v[26:27], v[18:19]
	v_lshlrev_b32_e32 v16, 16, v206
	v_and_b32_e32 v17, 0xffff0000, v206
	v_lshlrev_b32_e32 v18, 16, v207
	v_and_b32_e32 v19, 0xffff0000, v207
	v_pk_fma_f32 v[28:29], v[214:215], v[28:29], v[16:17]
	v_pk_fma_f32 v[30:31], v[214:215], v[30:31], v[18:19]
	v_lshlrev_b32_e32 v16, 16, v208
	v_and_b32_e32 v17, 0xffff0000, v208
	v_lshlrev_b32_e32 v18, 16, v209
	v_and_b32_e32 v19, 0xffff0000, v209
	v_pk_fma_f32 v[32:33], v[214:215], v[32:33], v[16:17]
	v_pk_fma_f32 v[34:35], v[214:215], v[34:35], v[18:19]
	v_lshlrev_b32_e32 v16, 16, v210
	v_and_b32_e32 v17, 0xffff0000, v210
	v_lshlrev_b32_e32 v18, 16, v211
	v_and_b32_e32 v19, 0xffff0000, v211
	v_pk_fma_f32 v[36:37], v[214:215], v[36:37], v[16:17]
	v_pk_fma_f32 v[38:39], v[214:215], v[38:39], v[18:19]
	v_lshlrev_b32_e32 v16, 16, v212
	v_and_b32_e32 v17, 0xffff0000, v212
	v_lshlrev_b32_e32 v18, 16, v213
	v_and_b32_e32 v19, 0xffff0000, v213
	v_pk_fma_f32 v[40:41], v[214:215], v[40:41], v[16:17]
	v_pk_fma_f32 v[42:43], v[214:215], v[42:43], v[18:19]
	s_lshl_b32 s38, s32, 6
	s_mul_i32 s38, s38, s18
	s_add_i32 s38, s38, s76
	s_cmp_eq_u32 s11, 6
	s_cbranch_scc1 .Lm20_s3_den
	s_mul_i32 s39, s38, 0x300
	v_add_u32_e32 v15, s39, v7
	v_cvt_pk_bf16_f32 v56, v56, v57
	v_cvt_pk_bf16_f32 v57, v58, v59
	global_store_dwordx2 v15, v[56:57], s[78:79]
	s_add_i32 s38, s38, s77
	s_mul_i32 s39, s38, 0x300
	v_add_u32_e32 v15, s39, v7
	v_cvt_pk_bf16_f32 v60, v60, v61
	v_cvt_pk_bf16_f32 v61, v62, v63
	global_store_dwordx2 v15, v[60:61], s[78:79]
	s_add_i32 s38, s38, s77
	s_mul_i32 s39, s38, 0x300
	v_add_u32_e32 v15, s39, v7
	v_cvt_pk_bf16_f32 v64, v64, v65
	v_cvt_pk_bf16_f32 v65, v66, v67
	global_store_dwordx2 v15, v[64:65], s[78:79]
	s_add_i32 s38, s38, s77
	s_mul_i32 s39, s38, 0x300
	v_add_u32_e32 v15, s39, v7
	v_cvt_pk_bf16_f32 v68, v68, v69
	v_cvt_pk_bf16_f32 v69, v70, v71
	global_store_dwordx2 v15, v[68:69], s[78:79]
	s_branch .Lm20_s3_od

; #define M2_FETCH(dst, c_) do { _Pragma("unroll") for (int i = 0; i < 12; ++i) dst[i] = __builtin_nontemporal_load((const u32x4_t*)(pkg0 + (size_t)(c_) * MLP_BYTES + MLP_QF + i * 1024 + lane * 16)); } while (0)
; DI void mlstm_m2_unit(const Args& A, LAS unsigned char* lds, int u, int tid, int wave, int lane) {
;     ...
;     if (wave == 7) {
;         u32x4_t f0[12], f1[12], f2[12];
;     ...
;         M2_FETCH(f0, 0); M2_FETCH(f1, 1);
;     ...
;         for (int c = 0; c < 32; c += 4) { M2_CHAIN(s0, c); M2_CHAIN(s1, c + 1); M2_CHAIN(s2, c + 2); M2_CHAIN(s3, c + 3); }
.Lm20_s3_od:
	s_add_i32 s30, s32, 4
	s_cmpk_lt_u32 s30, 0x20
	s_cbranch_scc0 .Lm20_s3_nold
	s_mul_i32 s27, s30, 0xbd00
	s_add_u32 s28, s14, s27
	s_addc_u32 s29, s15, 0
	global_load_dwordx2 v[194:195], v4, s[28:29] nt
	global_load_dwordx2 v[196:197], v4, s[28:29] offset:512 nt
	global_load_dwordx2 v[198:199], v4, s[28:29] offset:1024 nt
	global_load_dwordx2 v[200:201], v4, s[28:29] offset:1536 nt
	global_load_dwordx2 v[202:203], v5, s[28:29] nt
	global_load_dwordx2 v[204:205], v5, s[28:29] offset:512 nt
	global_load_dwordx2 v[206:207], v5, s[28:29] offset:1024 nt
	global_load_dwordx2 v[208:209], v5, s[28:29] offset:1536 nt
	global_load_dwordx2 v[210:211], v5, s[28:29] offset:2048 nt
	global_load_dwordx2 v[212:213], v5, s[28:29] offset:2560 nt
	global_load_dword v214, v6, s[28:29]
.Lm20_s3_nold:
	s_add_i32 s31, s31, 4
	s_cmpk_lt_u32 s31, 0x20
	s_cbranch_scc1 .Lm20_cloop
	s_branch .Lm20_uend
.Lm20_loader:
	v_lshlrev_b32_e32 v10, 4, v146
	v_mov_b32_e32 v11, 0
	s_mov_b64 s[42:43], 0x1000
	s_mov_b32 s30, 0
	s_mul_i32 s27, s30, 0xbd00
	s_add_u32 s28, s14, s27
	s_addc_u32 s29, s15, 0
	v_lshl_add_u64 v[12:13], s[28:29], 0, v[10:11]
	global_load_dwordx4 v[20:23], v[12:13], off nt
	global_load_dwordx4 v[24:27], v[12:13], off offset:1024 nt
	global_load_dwordx4 v[28:31], v[12:13], off offset:2048 nt
	global_load_dwordx4 v[32:35], v[12:13], off offset:3072 nt
	v_lshl_add_u64 v[12:13], v[12:13], 0, s[42:43]
	global_load_dwordx4 v[36:39], v[12:13], off nt
	global_load_dwordx4 v[40:43], v[12:13], off offset:1024 nt
	global_load_dwordx4 v[44:47], v[12:13], off offset:2048 nt
	global_load_dwordx4 v[48:51], v[12:13], off offset:3072 nt
	v_lshl_add_u64 v[12:13], v[12:13], 0, s[42:43]
	global_load_dwordx4 v[52:55], v[12:13], off nt
	global_load_dwordx4 v[56:59], v[12:13], off offset:1024 nt
	global_load_dwordx4 v[60:63], v[12:13], off offset:2048 nt
	global_load_dwordx4 v[64:67], v[12:13], off offset:3072 nt
	s_mov_b32 s30, 1
	s_mul_i32 s27, s30, 0xbd00
	s_add_u32 s28, s14, s27
	s_addc_u32 s29, s15, 0
	v_lshl_add_u64 v[12:13], s[28:29], 0, v[10:11]
	global_load_dwordx4 v[68:71], v[12:13], off nt
	global_load_dwordx4 v[72:75], v[12:13], off offset:1024 nt
	global_load_dwordx4 v[76:79], v[12:13], off offset:2048 nt
	global_load_dwordx4 v[80:83], v[12:13], off offset:3072 nt
	v_lshl_add_u64 v[12:13], v[12:13], 0, s[42:43]
	global_load_dwordx4 v[84:87], v[12:13], off nt
	global_load_dwordx4 v[88:91], v[12:13], off offset:1024 nt
	global_load_dwordx4 v[92:95], v[12:13], off offset:2048 nt
	global_load_dwordx4 v[96:99], v[12:13], off offset:3072 nt
	v_lshl_add_u64 v[12:13], v[12:13], 0, s[42:43]
	global_load_dwordx4 v[100:103], v[12:13], off nt
	global_load_dwordx4 v[104:107], v[12:13], off offset:1024 nt
	global_load_dwordx4 v[108:111], v[12:13], off offset:2048 nt
	global_load_dwordx4 v[112:115], v[12:13], off offset:3072 nt
	s_mov_b32 s30, 2
	s_mul_i32 s27, s30, 0xbd00
	s_add_u32 s28, s14, s27
	s_addc_u32 s29, s15, 0
	v_lshl_add_u64 v[12:13], s[28:29], 0, v[10:11]
	global_load_dwordx4 v[172:175], v[12:13], off nt
	global_load_dwordx4 v[176:179], v[12:13], off offset:1024 nt
	global_load_dwordx4 v[180:183], v[12:13], off offset:2048 nt
	global_load_dwordx4 v[184:187], v[12:13], off offset:3072 nt
	v_lshl_add_u64 v[12:13], v[12:13], 0, s[42:43]
	global_load_dwordx4 v[188:191], v[12:13], off nt
	global_load_dwordx4 v[192:195], v[12:13], off offset:1024 nt
	global_load_dwordx4 v[196:199], v[12:13], off offset:2048 nt
	global_load_dwordx4 v[200:203], v[12:13], off offset:3072 nt
	v_lshl_add_u64 v[12:13], v[12:13], 0, s[42:43]
	global_load_dwordx4 v[204:207], v[12:13], off nt
	global_load_dwordx4 v[208:211], v[12:13], off offset:1024 nt
	global_load_dwordx4 v[212:215], v[12:13], off offset:2048 nt
	global_load_dwordx4 v[216:219], v[12:13], off offset:3072 nt
	s_mov_b32 s30, 3
	s_mul_i32 s27, s30, 0xbd00
	s_add_u32 s28, s14, s27
	s_addc_u32 s29, s15, 0
	v_lshl_add_u64 v[12:13], s[28:29], 0, v[10:11]
	global_load_dwordx4 v[116:119], v[12:13], off nt
	global_load_dwordx4 v[120:123], v[12:13], off offset:1024 nt
	global_load_dwordx4 v[124:127], v[12:13], off offset:2048 nt
	global_load_dwordx4 v[128:131], v[12:13], off offset:3072 nt
	v_lshl_add_u64 v[12:13], v[12:13], 0, s[42:43]
	global_load_dwordx4 v[132:135], v[12:13], off nt
	global_load_dwordx4 v[136:139], v[12:13], off offset:1024 nt
	global_load_dwordx4 v[140:143], v[12:13], off offset:2048 nt
	global_load_dwordx4 v[148:151], v[12:13], off offset:3072 nt
	v_lshl_add_u64 v[12:13], v[12:13], 0, s[42:43]
	global_load_dwordx4 v[152:155], v[12:13], off nt
	global_load_dwordx4 v[156:159], v[12:13], off offset:1024 nt
	global_load_dwordx4 v[160:163], v[12:13], off offset:2048 nt
	global_load_dwordx4 v[164:167], v[12:13], off offset:3072 nt
	s_mov_b32 s31, 0
	s_mov_b32 s39, 7
; #define M2_FETCH(dst, c_) do { _Pragma("unroll") for (int i = 0; i < 12; ++i) dst[i] = __builtin_nontemporal_load((const u32x4_t*)(pkg0 + (size_t)(c_) * MLP_BYTES + MLP_QF + i * 1024 + lane * 16)); } while (0)
; DI void mlstm_m2_unit(const Args& A, LAS unsigned char* lds, int u, int tid, int wave, int lane) {
;     ...
;         M2_FETCH(f0, 0); M2_FETCH(f1, 1);
;         for (int c = 0; c < 30; c += 3) { M2_FETCH(f2, c + 2); M2_PUBLISH(f0, c); M2_FETCH(f0, c + 3); M2_PUBLISH(f1, c + 1); M2_FETCH(f1, c + 4); M2_PUBLISH(f2, c + 2); }
.Lm20_lloop:
	s_cmp_lt_i32 s31, 8
	s_cbranch_scc1 .Lm20_free0
	s_add_i32 s44, s31, -7
	s_mov_b32 s45, 0
	v_mov_b32_e32 v14, 0x18020
.Lm20_spin0:
	ds_read_b128 v[2:5], v14
	ds_read_b128 v[6:9], v14 offset:16
	s_waitcnt lgkmcnt(0)
	v_min3_u32 v2, v2, v3, v4
	v_min3_u32 v5, v5, v6, v7
	v_min3_u32 v2, v2, v5, v8
	v_cmp_le_u32_e32 vcc, s44, v2
	s_cbranch_vccnz .Lm20_free0
	s_add_i32 s45, s45, 1
	s_cmp_gt_u32 s45, 0x400000
	s_cbranch_scc1 .Lm20_free0
	s_sleep 1
	s_branch .Lm20_spin0
.Lm20_free0:
	s_and_b32 s46, s31, 7
	s_mul_i32 s47, s46, 0x3000
	v_add_u32_e32 v15, s47, v10
	s_waitcnt vmcnt(36)
	ds_write_b128 v15, v[20:23]
	ds_write_b128 v15, v[24:27] offset:1024
	ds_write_b128 v15, v[28:31] offset:2048
	ds_write_b128 v15, v[32:35] offset:3072
	ds_write_b128 v15, v[36:39] offset:4096
	ds_write_b128 v15, v[40:43] offset:5120
	ds_write_b128 v15, v[44:47] offset:6144
	ds_write_b128 v15, v[48:51] offset:7168
	ds_write_b128 v15, v[52:55] offset:8192
	ds_write_b128 v15, v[56:59] offset:9216
	ds_write_b128 v15, v[60:63] offset:10240
	ds_write_b128 v15, v[64:67] offset:11264
	s_lshl_b32 s46, s46, 2
	s_add_i32 s46, s46, 0x18000
	s_add_i32 s47, s31, 1
	v_mov_b32_e32 v16, s46
	v_mov_b32_e32 v17, s47
	s_waitcnt lgkmcnt(0)
	s_mov_b64 exec, s[72:73]
	ds_write_b32 v16, v17
	s_mov_b64 exec, -1
	s_add_i32 s30, s31, 4
	s_mul_i32 s27, s30, 0xbd00
	s_add_u32 s28, s14, s27
	s_addc_u32 s29, s15, 0
	v_lshl_add_u64 v[12:13], s[28:29], 0, v[10:11]
	global_load_dwordx4 v[20:23], v[12:13], off nt
	global_load_dwordx4 v[24:27], v[12:13], off offset:1024 nt
	global_load_dwordx4 v[28:31], v[12:13], off offset:2048 nt
	global_load_dwordx4 v[32:35], v[12:13], off offset:3072 nt
	v_lshl_add_u64 v[12:13], v[12:13], 0, s[42:43]
	global_load_dwordx4 v[36:39], v[12:13], off nt
	global_load_dwordx4 v[40:43], v[12:13], off offset:1024 nt
	global_load_dwordx4 v[44:47], v[12:13], off offset:2048 nt
	global_load_dwordx4 v[48:51], v[12:13], off offset:3072 nt
	v_lshl_add_u64 v[12:13], v[12:13], 0, s[42:43]
	global_load_dwordx4 v[52:55], v[12:13], off nt
	global_load_dwordx4 v[56:59], v[12:13], off offset:1024 nt
	global_load_dwordx4 v[60:63], v[12:13], off offset:2048 nt
	global_load_dwordx4 v[64:67], v[12:13], off offset:3072 nt
	s_add_i32 s31, s31, 1
	s_cmp_lt_i32 s31, 8
	s_cbranch_scc1 .Lm20_free1
	s_add_i32 s44, s31, -7
	s_mov_b32 s45, 0
	v_mov_b32_e32 v14, 0x18020

; #define M2_FETCH(dst, c_) do { _Pragma("unroll") for (int i = 0; i < 12; ++i) dst[i] = __builtin_nontemporal_load((const u32x4_t*)(pkg0 + (size_t)(c_) * MLP_BYTES + MLP_QF + i * 1024 + lane * 16)); } while (0)
; DI void mlstm_m2_unit(const Args& A, LAS unsigned char* lds, int u, int tid, int wave, int lane) {
;     ...
;         M2_FETCH(f0, 0); M2_FETCH(f1, 1);
;         for (int c = 0; c < 30; c += 3) { M2_FETCH(f2, c + 2); M2_PUBLISH(f0, c); M2_FETCH(f0, c + 3); M2_PUBLISH(f1, c + 1); M2_FETCH(f1, c + 4); M2_PUBLISH(f2, c + 2); }
.Lm20_free1:
	s_and_b32 s46, s31, 7
	s_mul_i32 s47, s46, 0x3000
	v_add_u32_e32 v15, s47, v10
	s_waitcnt vmcnt(36)
	ds_write_b128 v15, v[68:71]
	ds_write_b128 v15, v[72:75] offset:1024
	ds_write_b128 v15, v[76:79] offset:2048
	ds_write_b128 v15, v[80:83] offset:3072
	ds_write_b128 v15, v[84:87] offset:4096
	ds_write_b128 v15, v[88:91] offset:5120
	ds_write_b128 v15, v[92:95] offset:6144
	ds_write_b128 v15, v[96:99] offset:7168
	ds_write_b128 v15, v[100:103] offset:8192
	ds_write_b128 v15, v[104:107] offset:9216
	ds_write_b128 v15, v[108:111] offset:10240
	ds_write_b128 v15, v[112:115] offset:11264
	s_lshl_b32 s46, s46, 2
	s_add_i32 s46, s46, 0x18000
	s_add_i32 s47, s31, 1
	v_mov_b32_e32 v16, s46
	v_mov_b32_e32 v17, s47
	s_waitcnt lgkmcnt(0)
	s_mov_b64 exec, s[72:73]
	ds_write_b32 v16, v17
	s_mov_b64 exec, -1
	s_add_i32 s30, s31, 4
	s_mul_i32 s27, s30, 0xbd00
	s_add_u32 s28, s14, s27
	s_addc_u32 s29, s15, 0
	v_lshl_add_u64 v[12:13], s[28:29], 0, v[10:11]
	global_load_dwordx4 v[68:71], v[12:13], off nt
	global_load_dwordx4 v[72:75], v[12:13], off offset:1024 nt
	global_load_dwordx4 v[76:79], v[12:13], off offset:2048 nt
	global_load_dwordx4 v[80:83], v[12:13], off offset:3072 nt
	v_lshl_add_u64 v[12:13], v[12:13], 0, s[42:43]
	global_load_dwordx4 v[84:87], v[12:13], off nt
	global_load_dwordx4 v[88:91], v[12:13], off offset:1024 nt
	global_load_dwordx4 v[92:95], v[12:13], off offset:2048 nt
	global_load_dwordx4 v[96:99], v[12:13], off offset:3072 nt
	v_lshl_add_u64 v[12:13], v[12:13], 0, s[42:43]
	global_load_dwordx4 v[100:103], v[12:13], off nt
	global_load_dwordx4 v[104:107], v[12:13], off offset:1024 nt
	global_load_dwordx4 v[108:111], v[12:13], off offset:2048 nt
	global_load_dwordx4 v[112:115], v[12:13], off offset:3072 nt
	s_add_i32 s31, s31, 1
	s_cmp_lt_i32 s31, 8
	s_cbranch_scc1 .Lm20_free2
	s_add_i32 s44, s31, -7
	s_mov_b32 s45, 0
	v_mov_b32_e32 v14, 0x18020

; #define M2_FETCH(dst, c_) do { _Pragma("unroll") for (int i = 0; i < 12; ++i) dst[i] = __builtin_nontemporal_load((const u32x4_t*)(pkg0 + (size_t)(c_) * MLP_BYTES + MLP_QF + i * 1024 + lane * 16)); } while (0)
; DI void mlstm_m2_unit(const Args& A, LAS unsigned char* lds, int u, int tid, int wave, int lane) {
;     ...
;         M2_FETCH(f0, 0); M2_FETCH(f1, 1);
;         for (int c = 0; c < 30; c += 3) { M2_FETCH(f2, c + 2); M2_PUBLISH(f0, c); M2_FETCH(f0, c + 3); M2_PUBLISH(f1, c + 1); M2_FETCH(f1, c + 4); M2_PUBLISH(f2, c + 2); }
.Lm20_free2:
	s_and_b32 s46, s31, 7
	s_mul_i32 s47, s46, 0x3000
	v_add_u32_e32 v15, s47, v10
	s_waitcnt vmcnt(36)
	ds_write_b128 v15, v[172:175]
	ds_write_b128 v15, v[176:179] offset:1024
	ds_write_b128 v15, v[180:183] offset:2048
	ds_write_b128 v15, v[184:187] offset:3072
	ds_write_b128 v15, v[188:191] offset:4096
	ds_write_b128 v15, v[192:195] offset:5120
	ds_write_b128 v15, v[196:199] offset:6144
	ds_write_b128 v15, v[200:203] offset:7168
	ds_write_b128 v15, v[204:207] offset:8192
	ds_write_b128 v15, v[208:211] offset:9216
	ds_write_b128 v15, v[212:215] offset:10240
	ds_write_b128 v15, v[216:219] offset:11264
	s_lshl_b32 s46, s46, 2
	s_add_i32 s46, s46, 0x18000
	s_add_i32 s47, s31, 1
	v_mov_b32_e32 v16, s46
	v_mov_b32_e32 v17, s47
	s_waitcnt lgkmcnt(0)
	s_mov_b64 exec, s[72:73]
	ds_write_b32 v16, v17
	s_mov_b64 exec, -1
	s_add_i32 s30, s31, 4
	s_mul_i32 s27, s30, 0xbd00
	s_add_u32 s28, s14, s27
	s_addc_u32 s29, s15, 0
	v_lshl_add_u64 v[12:13], s[28:29], 0, v[10:11]
	global_load_dwordx4 v[172:175], v[12:13], off nt
	global_load_dwordx4 v[176:179], v[12:13], off offset:1024 nt
	global_load_dwordx4 v[180:183], v[12:13], off offset:2048 nt
	global_load_dwordx4 v[184:187], v[12:13], off offset:3072 nt
	v_lshl_add_u64 v[12:13], v[12:13], 0, s[42:43]
	global_load_dwordx4 v[188:191], v[12:13], off nt
	global_load_dwordx4 v[192:195], v[12:13], off offset:1024 nt
	global_load_dwordx4 v[196:199], v[12:13], off offset:2048 nt
	global_load_dwordx4 v[200:203], v[12:13], off offset:3072 nt
	v_lshl_add_u64 v[12:13], v[12:13], 0, s[42:43]
	global_load_dwordx4 v[204:207], v[12:13], off nt
	global_load_dwordx4 v[208:211], v[12:13], off offset:1024 nt
	global_load_dwordx4 v[212:215], v[12:13], off offset:2048 nt
	global_load_dwordx4 v[216:219], v[12:13], off offset:3072 nt
	s_add_i32 s31, s31, 1
	s_cmp_lt_i32 s31, 8
	s_cbranch_scc1 .Lm20_free3
	s_add_i32 s44, s31, -7
	s_mov_b32 s45, 0
	v_mov_b32_e32 v14, 0x18020

; #define M2_FETCH(dst, c_) do { _Pragma("unroll") for (int i = 0; i < 12; ++i) dst[i] = __builtin_nontemporal_load((const u32x4_t*)(pkg0 + (size_t)(c_) * MLP_BYTES + MLP_QF + i * 1024 + lane * 16)); } while (0)
; DI void mlstm_m2_unit(const Args& A, LAS unsigned char* lds, int u, int tid, int wave, int lane) {
;     ...
;         M2_FETCH(f0, 0); M2_FETCH(f1, 1);
;         for (int c = 0; c < 30; c += 3) { M2_FETCH(f2, c + 2); M2_PUBLISH(f0, c); M2_FETCH(f0, c + 3); M2_PUBLISH(f1, c + 1); M2_FETCH(f1, c + 4); M2_PUBLISH(f2, c + 2); }
.Lm20_free3:
	s_and_b32 s46, s31, 7
	s_mul_i32 s47, s46, 0x3000
	v_add_u32_e32 v15, s47, v10
	s_waitcnt vmcnt(36)
	ds_write_b128 v15, v[116:119]
	ds_write_b128 v15, v[120:123] offset:1024
	ds_write_b128 v15, v[124:127] offset:2048
	ds_write_b128 v15, v[128:131] offset:3072
	ds_write_b128 v15, v[132:135] offset:4096
	ds_write_b128 v15, v[136:139] offset:5120
	ds_write_b128 v15, v[140:143] offset:6144
	ds_write_b128 v15, v[148:151] offset:7168
	ds_write_b128 v15, v[152:155] offset:8192
	ds_write_b128 v15, v[156:159] offset:9216
	ds_write_b128 v15, v[160:163] offset:10240
	ds_write_b128 v15, v[164:167] offset:11264
	s_lshl_b32 s46, s46, 2
	s_add_i32 s46, s46, 0x18000
	s_add_i32 s47, s31, 1
	v_mov_b32_e32 v16, s46
	v_mov_b32_e32 v17, s47
	s_waitcnt lgkmcnt(0)
	s_mov_b64 exec, s[72:73]
	ds_write_b32 v16, v17
	s_mov_b64 exec, -1
	s_add_i32 s30, s31, 4
	s_mul_i32 s27, s30, 0xbd00
	s_add_u32 s28, s14, s27
	s_addc_u32 s29, s15, 0
	v_lshl_add_u64 v[12:13], s[28:29], 0, v[10:11]
	global_load_dwordx4 v[116:119], v[12:13], off nt
	global_load_dwordx4 v[120:123], v[12:13], off offset:1024 nt
	global_load_dwordx4 v[124:127], v[12:13], off offset:2048 nt
	global_load_dwordx4 v[128:131], v[12:13], off offset:3072 nt
	v_lshl_add_u64 v[12:13], v[12:13], 0, s[42:43]
	global_load_dwordx4 v[132:135], v[12:13], off nt
	global_load_dwordx4 v[136:139], v[12:13], off offset:1024 nt
	global_load_dwordx4 v[140:143], v[12:13], off offset:2048 nt
	global_load_dwordx4 v[148:151], v[12:13], off offset:3072 nt
	v_lshl_add_u64 v[12:13], v[12:13], 0, s[42:43]
	global_load_dwordx4 v[152:155], v[12:13], off nt
	global_load_dwordx4 v[156:159], v[12:13], off offset:1024 nt
	global_load_dwordx4 v[160:163], v[12:13], off offset:2048 nt
	global_load_dwordx4 v[164:167], v[12:13], off offset:3072 nt
	s_add_i32 s31, s31, 1
	s_add_i32 s39, s39, -1
	s_cmp_lg_u32 s39, 0
	s_cbranch_scc1 .Lm20_lloop
	s_cmp_lt_i32 s31, 8
	s_cbranch_scc1 .Lm20_free4
	s_add_i32 s44, s31, -7
	s_mov_b32 s45, 0
	v_mov_b32_e32 v14, 0x18020

.Lm20_free4:
	s_and_b32 s46, s31, 7
	s_mul_i32 s47, s46, 0x3000
	v_add_u32_e32 v15, s47, v10
	s_waitcnt vmcnt(36)
	ds_write_b128 v15, v[20:23]
	ds_write_b128 v15, v[24:27] offset:1024
	ds_write_b128 v15, v[28:31] offset:2048
	ds_write_b128 v15, v[32:35] offset:3072
	ds_write_b128 v15, v[36:39] offset:4096
	ds_write_b128 v15, v[40:43] offset:5120
	ds_write_b128 v15, v[44:47] offset:6144
	ds_write_b128 v15, v[48:51] offset:7168
	ds_write_b128 v15, v[52:55] offset:8192
	ds_write_b128 v15, v[56:59] offset:9216
	ds_write_b128 v15, v[60:63] offset:10240
	ds_write_b128 v15, v[64:67] offset:11264
	s_lshl_b32 s46, s46, 2
	s_add_i32 s46, s46, 0x18000
	s_add_i32 s47, s31, 1
	v_mov_b32_e32 v16, s46
	v_mov_b32_e32 v17, s47
	s_waitcnt lgkmcnt(0)
	s_mov_b64 exec, s[72:73]
	ds_write_b32 v16, v17
	s_mov_b64 exec, -1
	s_add_i32 s31, s31, 1
	s_cmp_lt_i32 s31, 8
	s_cbranch_scc1 .Lm20_free5
	s_add_i32 s44, s31, -7
	s_mov_b32 s45, 0
	v_mov_b32_e32 v14, 0x18020

.Lm20_free5:
	s_and_b32 s46, s31, 7
	s_mul_i32 s47, s46, 0x3000
	v_add_u32_e32 v15, s47, v10
	s_waitcnt vmcnt(24)
	ds_write_b128 v15, v[68:71]
	ds_write_b128 v15, v[72:75] offset:1024
	ds_write_b128 v15, v[76:79] offset:2048
	ds_write_b128 v15, v[80:83] offset:3072
	ds_write_b128 v15, v[84:87] offset:4096
	ds_write_b128 v15, v[88:91] offset:5120
	ds_write_b128 v15, v[92:95] offset:6144
	ds_write_b128 v15, v[96:99] offset:7168
	ds_write_b128 v15, v[100:103] offset:8192
	ds_write_b128 v15, v[104:107] offset:9216
	ds_write_b128 v15, v[108:111] offset:10240
	ds_write_b128 v15, v[112:115] offset:11264
	s_lshl_b32 s46, s46, 2
	s_add_i32 s46, s46, 0x18000
	s_add_i32 s47, s31, 1
	v_mov_b32_e32 v16, s46
	v_mov_b32_e32 v17, s47
	s_waitcnt lgkmcnt(0)
	s_mov_b64 exec, s[72:73]
	ds_write_b32 v16, v17
	s_mov_b64 exec, -1
	s_add_i32 s31, s31, 1
	s_cmp_lt_i32 s31, 8
	s_cbranch_scc1 .Lm20_free6
	s_add_i32 s44, s31, -7
	s_mov_b32 s45, 0
	v_mov_b32_e32 v14, 0x18020

.Lm20_free6:
	s_and_b32 s46, s31, 7
	s_mul_i32 s47, s46, 0x3000
	v_add_u32_e32 v15, s47, v10
	s_waitcnt vmcnt(12)
	ds_write_b128 v15, v[172:175]
	ds_write_b128 v15, v[176:179] offset:1024
	ds_write_b128 v15, v[180:183] offset:2048
	ds_write_b128 v15, v[184:187] offset:3072
	ds_write_b128 v15, v[188:191] offset:4096
	ds_write_b128 v15, v[192:195] offset:5120
	ds_write_b128 v15, v[196:199] offset:6144
	ds_write_b128 v15, v[200:203] offset:7168
	ds_write_b128 v15, v[204:207] offset:8192
	ds_write_b128 v15, v[208:211] offset:9216
	ds_write_b128 v15, v[212:215] offset:10240
	ds_write_b128 v15, v[216:219] offset:11264
	s_lshl_b32 s46, s46, 2
	s_add_i32 s46, s46, 0x18000
	s_add_i32 s47, s31, 1
	v_mov_b32_e32 v16, s46
	v_mov_b32_e32 v17, s47
	s_waitcnt lgkmcnt(0)
	s_mov_b64 exec, s[72:73]
	ds_write_b32 v16, v17
	s_mov_b64 exec, -1
	s_add_i32 s31, s31, 1
	s_cmp_lt_i32 s31, 8
	s_cbranch_scc1 .Lm20_free7
	s_add_i32 s44, s31, -7
	s_mov_b32 s45, 0
	v_mov_b32_e32 v14, 0x18020

.Lm20_free7:
	s_and_b32 s46, s31, 7
	s_mul_i32 s47, s46, 0x3000
	v_add_u32_e32 v15, s47, v10
	s_waitcnt vmcnt(0)
	ds_write_b128 v15, v[116:119]
	ds_write_b128 v15, v[120:123] offset:1024
	ds_write_b128 v15, v[124:127] offset:2048
	ds_write_b128 v15, v[128:131] offset:3072
	ds_write_b128 v15, v[132:135] offset:4096
	ds_write_b128 v15, v[136:139] offset:5120
	ds_write_b128 v15, v[140:143] offset:6144
	ds_write_b128 v15, v[148:151] offset:7168
	ds_write_b128 v15, v[152:155] offset:8192
	ds_write_b128 v15, v[156:159] offset:9216
	ds_write_b128 v15, v[160:163] offset:10240
	ds_write_b128 v15, v[164:167] offset:11264
	s_lshl_b32 s46, s46, 2
	s_add_i32 s46, s46, 0x18000
	s_add_i32 s47, s31, 1
	v_mov_b32_e32 v16, s46
	v_mov_b32_e32 v17, s47
	s_waitcnt lgkmcnt(0)
	s_mov_b64 exec, s[72:73]
	ds_write_b32 v16, v17
	s_mov_b64 exec, -1
	s_add_i32 s31, s31, 1

; template <int l> DI void run_layer(const Args& A, LAS unsigned char* lds, const XcdBarrier& bar, int lo, int hi, int G, int bid, int tid, int lane, int wave, int gw, int ngw, int gtid, int nthr) {
;     ...
;           for (int rep = 0; rep < 1 + ((MK_DUP >> 15) & 1); ++rep) for (int u = bid; u < 96 + 64; u += G) { if (u >= 96) mlstm_m2_unit(A, lds, u - 96, tid, wave, lane); });
.Lm20_unext:
	s_add_i32 s6, s6, s50
	s_branch .Lm20_uloop
